# LN row loop: static s_setprio 1 for waves 4-7 as in PEER (attention phase left at default priority: raising it there was slower)
# speedup vs baseline: 1.0088x; 1.0029x over previous
.LBB0_502:
	s_andn2_b64 vcc, exec, s[0:1]
	s_cbranch_vccnz .LBB0_595
	s_waitcnt vmcnt(0)
	v_mov_b32_e32 v8, v0
	s_nop 0
	v_readfirstlane_b32 s0, v8
	s_ashr_i32 s50, s0, 6
	s_cmp_gt_u32 s50, 3
	s_cbranch_scc0 .Lln_lowprio
	s_setprio 1
.Lln_lowprio:
	s_nop 0
	s_mul_i32 s0, s50, s33
	s_add_i32 s52, s0, s2
	s_nop 0
	s_mov_b64 s[0:1], s[96:97]
	s_load_dwordx2 s[4:5], s[0:1], 0xa8
	v_and_b32_e32 v68, 63, v8
	s_cmp_lt_i32 s52, s26
	s_cselect_b64 s[42:43], -1, 0
	s_cmp_ge_i32 s52, s26
	v_lshlrev_b32_e32 v144, 3, v68
	v_lshlrev_b32_e32 v2, 4, v68
	s_cbranch_scc1 .LBB0_512
	s_ashr_i32 s53, s52, 31
	s_lshl_b64 s[8:9], s[52:53], 11
	s_waitcnt lgkmcnt(0)
	s_add_u32 s8, s4, s8
	s_addc_u32 s9, s5, s9
	v_mov_b32_e32 v145, v3
	v_lshl_add_u64 v[6:7], s[8:9], 0, v[144:145]
	v_add_co_u32_e32 v4, vcc, 0x17600000, v6
	s_cmp_lg_u32 s36, 0
	s_nop 0
	v_addc_co_u32_e32 v5, vcc, 0, v7, vcc
	global_load_dwordx2 v[170:171], v[4:5], off
	s_cselect_b64 s[8:9], -1, 0
	s_lshl_b64 s[40:41], s[52:53], 12
	s_add_u32 s40, s4, s40
	s_addc_u32 s41, s5, s41
	v_lshl_add_u64 v[4:5], s[40:41], 0, v[2:3]
	s_mov_b64 s[40:41], 0xb000000
	s_cmp_eq_u32 s36, 0
	v_lshl_add_u64 v[4:5], v[4:5], 0, s[40:41]
	s_cbranch_scc1 .LBB0_506
	global_load_dwordx4 v[96:99], v[4:5], off

.LBB0_595:
	s_setprio 0
	s_nop 0
	s_cmp_le_i32 s68, s6
	s_cselect_b64 s[0:1], -1, 0
	s_cmp_lt_i32 s6, s69
	s_cselect_b64 s[4:5], -1, 0
	s_and_b64 s[4:5], s[0:1], s[4:5]
	s_mov_b64 s[0:1], -1
	s_and_b64 vcc, exec, s[4:5]
	s_cbranch_vccnz .LBB0_597
	s_mul_i32 s0, s36, 6
	s_add_i32 s6, s0, 7
	s_mov_b64 s[0:1], 0
